# loop-edge edits (back-edge rotation): loop-carried copy and counter update moved in front of the closing barrier, exit test only in the copy that can exit, transition test only in the copy that can re
# baseline (speedup 1.0000x reference)
.LBB0_792:
	v_exp_f32_e32 v197, v96
	v_exp_f32_e32 v208, v97
	v_exp_f32_e32 v209, v98
	v_exp_f32_e32 v210, v99
	v_exp_f32_e32 v211, v100
	v_exp_f32_e32 v220, v101
	v_exp_f32_e32 v221, v102
	v_exp_f32_e32 v222, v103
	v_exp_f32_e32 v223, v104
	v_exp_f32_e32 v224, v105
	v_exp_f32_e32 v225, v106
	v_exp_f32_e32 v226, v107
	v_exp_f32_e32 v227, v108
	v_exp_f32_e32 v228, v109
	v_exp_f32_e32 v229, v110
	v_exp_f32_e32 v230, v111
	s_waitcnt vmcnt(4) lgkmcnt(0)
	s_barrier
	ds_read_b128 v[64:67], v134 offset:50176
	ds_read_b128 v[68:71], v134 offset:58368
	ds_read_b128 v[200:203], v135 offset:50176
	ds_read_b128 v[204:207], v135 offset:58368
	v_exp_f32_e32 v231, v87
	s_waitcnt lgkmcnt(2)
	v_mfma_f32_32x32x16_bf16 v[96:111], v[64:67], v[122:125], 0
	v_exp_f32_e32 v232, v88
	v_exp_f32_e32 v233, v89
	v_exp_f32_e32 v234, v90
	v_exp_f32_e32 v235, v91
	v_exp_f32_e32 v236, v92
	v_exp_f32_e32 v237, v93
	v_exp_f32_e32 v238, v94
	v_mfma_f32_32x32x16_bf16 v[64:79], v[68:71], v[122:125], 0
	v_exp_f32_e32 v95, v95
	s_waitcnt lgkmcnt(0)
	v_mfma_f32_32x32x16_bf16 v[96:111], v[200:203], v[126:129], v[96:111]
	v_mfma_f32_32x32x16_bf16 v[64:79], v[204:207], v[126:129], v[64:79]
	ds_read_b128 v[200:203], v136 offset:50176
	ds_read_b128 v[204:207], v136 offset:58368
	s_waitcnt lgkmcnt(0)
	v_mfma_f32_32x32x16_bf16 v[96:111], v[200:203], v[118:121], v[96:111]
	v_mfma_f32_32x32x16_bf16 v[64:79], v[204:207], v[118:121], v[64:79]
	ds_read_b128 v[200:203], v137 offset:50176
	ds_read_b128 v[204:207], v137 offset:58368
	s_waitcnt lgkmcnt(0)
	v_mfma_f32_32x32x16_bf16 v[96:111], v[200:203], v[114:117], v[96:111]
	v_exp_f32_e32 v201, v80
	v_add_f32_e32 v80, v208, v197
	v_add_f32_e32 v199, v209, v210
	v_add_f32_e32 v80, v211, v80
	v_add_f32_e32 v199, v220, v199
	v_add_f32_e32 v80, v221, v80
	v_add_f32_e32 v199, v222, v199
	v_add_f32_e32 v80, v223, v80
	v_add_f32_e32 v199, v224, v199
	v_add_f32_e32 v80, v225, v80
	v_add_f32_e32 v199, v226, v199
	v_add_f32_e32 v80, v227, v80
	v_exp_f32_e32 v202, v81
	v_add_f32_e32 v199, v228, v199
	v_exp_f32_e32 v203, v82
	v_add_f32_e32 v80, v229, v80
	v_mfma_f32_32x32x16_bf16 v[64:79], v[204:207], v[114:117], v[64:79]
	v_exp_f32_e32 v204, v83
	v_add_f32_e32 v199, v230, v199
	v_exp_f32_e32 v205, v84
	v_add_f32_e32 v80, v201, v80
	v_exp_f32_e32 v206, v85
	v_add_f32_e32 v199, v202, v199
	v_exp_f32_e32 v207, v86
	v_add_f32_e32 v80, v203, v80
	v_add_f32_e32 v199, v204, v199
	v_add_f32_e32 v80, v205, v80
	v_add_f32_e32 v199, v206, v199
	v_add_f32_e32 v80, v207, v80
	v_add_f32_e32 v199, v231, v199
	v_add_f32_e32 v80, v232, v80
	v_add_f32_e32 v199, v233, v199
	v_add_f32_e32 v80, v234, v80
	v_add_f32_e32 v199, v235, v199
	v_add_f32_e32 v80, v236, v80
	v_add_f32_e32 v199, v237, v199
	v_add_f32_e32 v80, v238, v80
	v_add_f32_e32 v199, v95, v199
	v_add_f32_e32 v199, v199, v80
	v_cvt_pk_bf16_f32 v80, v197, v208
	v_cvt_pk_bf16_f32 v81, v209, v210
	v_cvt_pk_bf16_f32 v82, v211, v220
	v_cvt_pk_bf16_f32 v83, v221, v222
	v_cvt_pk_bf16_f32 v84, v223, v224
	v_cvt_pk_bf16_f32 v85, v225, v226
	v_cvt_pk_bf16_f32 v86, v227, v228
	v_cvt_pk_bf16_f32 v87, v229, v230
	v_cvt_pk_bf16_f32 v88, v201, v202
	v_cvt_pk_bf16_f32 v89, v203, v204
	v_cvt_pk_bf16_f32 v90, v205, v206
	v_cvt_pk_bf16_f32 v91, v207, v231
	v_cvt_pk_bf16_f32 v92, v232, v233
	v_cvt_pk_bf16_f32 v93, v234, v235
	v_cvt_pk_bf16_f32 v94, v236, v237
	v_cvt_pk_bf16_f32 v95, v238, v95
	s_add_i32 m0, s84, 0x400
	s_add_u32 s66, s78, s65
	s_addc_u32 s67, s79, 0
	global_load_lds_dwordx4 v185, s[66:67]
	s_add_i32 m0, s84, 0x2400
	s_add_i32 s64, s65, 0x60000
	global_load_lds_dwordx4 v184, s[66:67]
	s_add_i32 m0, s84, 0x10400
	s_add_u32 s70, s80, s64
	s_addc_u32 s71, s81, 0
	global_load_lds_dwordx4 v183, s[70:71]
	s_add_i32 m0, s84, 0x12400
	s_mov_b32 s65, s64
	global_load_lds_dwordx4 v182, s[70:71]

.LBB0_799:
	v_exp_f32_e32 v159, v96
	v_exp_f32_e32 v161, v97
	v_exp_f32_e32 v157, v98
	v_exp_f32_e32 v160, v99
	v_exp_f32_e32 v155, v100
	v_exp_f32_e32 v158, v101
	v_exp_f32_e32 v154, v102
	v_exp_f32_e32 v156, v103
	v_exp_f32_e32 v151, v104
	v_exp_f32_e32 v153, v105
	v_exp_f32_e32 v149, v106
	v_exp_f32_e32 v152, v107
	v_exp_f32_e32 v147, v108
	v_exp_f32_e32 v150, v109
	v_exp_f32_e32 v146, v110
	v_exp_f32_e32 v148, v111
	v_fma_f32 v80, v193, v179, v195
	v_fma_f32 v179, v80, v198, v199
	v_mov_b32_e32 v193, v197
	s_waitcnt vmcnt(4) lgkmcnt(0)
	s_barrier
	ds_read_b128 v[80:83], v130 offset:50176
	ds_read_b128 v[84:87], v130 offset:58368
	ds_read_b128 v[196:199], v131 offset:50176
	ds_read_b128 v[200:203], v131 offset:58368
	s_waitcnt lgkmcnt(2)
	v_mfma_f32_32x32x16_bf16 v[96:111], v[80:83], v[122:125], 0
	v_exp_f32_e32 v204, v72
	v_exp_f32_e32 v205, v73
	v_exp_f32_e32 v206, v74
	v_exp_f32_e32 v207, v75
	v_exp_f32_e32 v208, v76
	v_exp_f32_e32 v209, v77
	v_mfma_f32_32x32x16_bf16 v[80:95], v[84:87], v[122:125], 0
	v_exp_f32_e32 v210, v78
	v_exp_f32_e32 v79, v79
	s_waitcnt lgkmcnt(0)
	v_mfma_f32_32x32x16_bf16 v[96:111], v[196:199], v[126:129], v[96:111]
	v_mfma_f32_32x32x16_bf16 v[80:95], v[200:203], v[126:129], v[80:95]
	ds_read_b128 v[196:199], v132 offset:50176
	ds_read_b128 v[200:203], v132 offset:58368
	s_waitcnt lgkmcnt(0)
	v_mfma_f32_32x32x16_bf16 v[96:111], v[196:199], v[118:121], v[96:111]
	v_mfma_f32_32x32x16_bf16 v[80:95], v[200:203], v[118:121], v[80:95]
	ds_read_b128 v[196:199], v133 offset:50176
	ds_read_b128 v[200:203], v133 offset:58368
	v_exp_f32_e32 v180, v64
	v_add_f32_e32 v64, v161, v159
	v_add_f32_e32 v195, v157, v160
	v_add_f32_e32 v64, v155, v64
	v_add_f32_e32 v195, v158, v195
	v_add_f32_e32 v64, v154, v64
	v_add_f32_e32 v195, v156, v195
	v_add_f32_e32 v64, v151, v64
	v_add_f32_e32 v195, v153, v195
	v_add_f32_e32 v64, v149, v64
	v_add_f32_e32 v195, v152, v195
	v_add_f32_e32 v64, v147, v64
	s_waitcnt lgkmcnt(0)
	v_mfma_f32_32x32x16_bf16 v[96:111], v[196:199], v[114:117], v[96:111]
	v_exp_f32_e32 v197, v65
	v_add_f32_e32 v195, v150, v195
	v_exp_f32_e32 v198, v66
	v_add_f32_e32 v64, v146, v64
	v_exp_f32_e32 v199, v67
	v_add_f32_e32 v195, v148, v195
	v_add_f32_e32 v64, v180, v64
	v_mfma_f32_32x32x16_bf16 v[80:95], v[200:203], v[114:117], v[80:95]
	v_exp_f32_e32 v200, v68
	v_exp_f32_e32 v201, v69
	v_add_f32_e32 v195, v197, v195
	v_exp_f32_e32 v202, v70
	v_add_f32_e32 v64, v198, v64
	v_exp_f32_e32 v203, v71
	v_add_f32_e32 v195, v199, v195
	v_add_f32_e32 v64, v200, v64
	v_add_f32_e32 v195, v201, v195
	v_add_f32_e32 v64, v202, v64
	v_add_f32_e32 v195, v203, v195
	v_add_f32_e32 v64, v204, v64
	v_add_f32_e32 v195, v205, v195
	v_add_f32_e32 v64, v206, v64
	v_add_f32_e32 v195, v207, v195
	v_add_f32_e32 v64, v208, v64
	v_add_f32_e32 v195, v209, v195
	v_add_f32_e32 v64, v210, v64
	v_add_f32_e32 v195, v79, v195
	v_add_f32_e32 v195, v195, v64
	v_cvt_pk_bf16_f32 v64, v159, v161
	v_cvt_pk_bf16_f32 v65, v157, v160
	v_cvt_pk_bf16_f32 v66, v155, v158
	v_cvt_pk_bf16_f32 v67, v154, v156
	v_cvt_pk_bf16_f32 v68, v151, v153
	v_cvt_pk_bf16_f32 v69, v149, v152
	v_cvt_pk_bf16_f32 v70, v147, v150
	v_cvt_pk_bf16_f32 v71, v146, v148
	v_cvt_pk_bf16_f32 v72, v180, v197
	v_cvt_pk_bf16_f32 v73, v198, v199
	v_cvt_pk_bf16_f32 v74, v200, v201
	v_cvt_pk_bf16_f32 v75, v202, v203
	v_cvt_pk_bf16_f32 v76, v204, v205
	v_cvt_pk_bf16_f32 v77, v206, v207
	v_cvt_pk_bf16_f32 v78, v208, v209
	v_cvt_pk_bf16_f32 v79, v210, v79
	s_add_i32 m0, s84, 0x4400
	s_add_u32 s66, s78, s65
	s_addc_u32 s67, s79, 0
	global_load_lds_dwordx4 v185, s[66:67]
	s_add_i32 m0, s84, 0x6400
	s_add_i32 s64, s65, 0x60000
	global_load_lds_dwordx4 v184, s[66:67]
	s_add_i32 m0, s84, 0x14400
	s_add_u32 s70, s80, s64
	s_addc_u32 s71, s81, 0
	global_load_lds_dwordx4 v183, s[70:71]
	s_add_i32 m0, s84, 0x16400
	s_mov_b32 s65, s64
	global_load_lds_dwordx4 v182, s[70:71]
	ds_read_b64_tr_b16 v[198:199], v192 offset:33792
	ds_read_b64_tr_b16 v[200:201], v192 offset:35840
	ds_read_b64_tr_b16 v[202:203], v192 offset:37888
	ds_read_b64_tr_b16 v[204:205], v192 offset:39936
	ds_read_b64_tr_b16 v[206:207], v192 offset:41984
	ds_read_b64_tr_b16 v[208:209], v192 offset:44032
	ds_read_b64_tr_b16 v[222:223], v192 offset:46080
	ds_read_b64_tr_b16 v[224:225], v192 offset:48128
	s_waitcnt lgkmcnt(0)
	v_mfma_f32_32x32x16_bf16 v[0:15], v[64:67], v[198:201], v[0:15]
	ds_read_b64_tr_b16 v[198:199], v192 offset:34304
	ds_read_b64_tr_b16 v[200:201], v192 offset:36352
	v_mfma_f32_32x32x16_bf16 v[0:15], v[68:71], v[202:205], v[0:15]
	ds_read_b64_tr_b16 v[202:203], v192 offset:38400
	ds_read_b64_tr_b16 v[204:205], v192 offset:40448
	v_mfma_f32_32x32x16_bf16 v[0:15], v[72:75], v[206:209], v[0:15]
	ds_read_b64_tr_b16 v[206:207], v192 offset:42496
	ds_read_b64_tr_b16 v[208:209], v192 offset:44544
	v_mfma_f32_32x32x16_bf16 v[0:15], v[76:79], v[222:225], v[0:15]
	ds_read_b64_tr_b16 v[222:223], v192 offset:46592
	ds_read_b64_tr_b16 v[224:225], v192 offset:48640
	s_waitcnt lgkmcnt(0)
	v_mfma_f32_32x32x16_bf16 v[48:63], v[64:67], v[198:201], v[48:63]
	ds_read_b64_tr_b16 v[198:199], v192 offset:34816
	ds_read_b64_tr_b16 v[200:201], v192 offset:36864
	v_mfma_f32_32x32x16_bf16 v[48:63], v[68:71], v[202:205], v[48:63]
	ds_read_b64_tr_b16 v[202:203], v192 offset:38912
	ds_read_b64_tr_b16 v[204:205], v192 offset:40960
	v_mfma_f32_32x32x16_bf16 v[48:63], v[72:75], v[206:209], v[48:63]
	ds_read_b64_tr_b16 v[206:207], v192 offset:43008
	ds_read_b64_tr_b16 v[208:209], v192 offset:45056
	v_mfma_f32_32x32x16_bf16 v[48:63], v[76:79], v[222:225], v[48:63]
	ds_read_b64_tr_b16 v[222:223], v192 offset:47104
	ds_read_b64_tr_b16 v[224:225], v192 offset:49152
	s_waitcnt lgkmcnt(0)
	v_mfma_f32_32x32x16_bf16 v[32:47], v[64:67], v[198:201], v[32:47]
	ds_read_b64_tr_b16 v[198:199], v192 offset:35328
	ds_read_b64_tr_b16 v[200:201], v192 offset:37376
	v_mfma_f32_32x32x16_bf16 v[32:47], v[68:71], v[202:205], v[32:47]
	ds_read_b64_tr_b16 v[202:203], v192 offset:39424
	ds_read_b64_tr_b16 v[204:205], v192 offset:41472
	v_mfma_f32_32x32x16_bf16 v[32:47], v[72:75], v[206:209], v[32:47]
	ds_read_b64_tr_b16 v[206:207], v192 offset:43520
	ds_read_b64_tr_b16 v[208:209], v192 offset:45568
	v_mfma_f32_32x32x16_bf16 v[32:47], v[76:79], v[222:225], v[32:47]
	ds_read_b64_tr_b16 v[222:223], v192 offset:47616
	ds_read_b64_tr_b16 v[224:225], v192 offset:49664
	s_waitcnt lgkmcnt(0)
	v_mfma_f32_32x32x16_bf16 v[16:31], v[64:67], v[198:201], v[16:31]
	v_max_f32_e32 v64, v96, v97
	v_max3_f32 v65, v80, v81, v82
	v_max3_f32 v64, v64, v98, v99
	v_max3_f32 v65, v65, v83, v84
	v_max3_f32 v64, v64, v100, v101
	v_mfma_f32_32x32x16_bf16 v[16:31], v[68:71], v[202:205], v[16:31]
	v_max3_f32 v65, v65, v85, v86
	v_max3_f32 v64, v64, v102, v103
	v_max3_f32 v65, v65, v87, v88
	v_max3_f32 v64, v64, v104, v105
	v_max3_f32 v65, v65, v89, v90
	v_max3_f32 v64, v64, v106, v107
	v_max3_f32 v65, v65, v91, v92
	v_mfma_f32_32x32x16_bf16 v[16:31], v[72:75], v[206:209], v[16:31]
	v_max3_f32 v64, v64, v108, v109
	v_max3_f32 v65, v65, v93, v94
	v_max3_f32 v64, v64, v110, v111
	v_max3_f32 v64, v64, v65, v95
	v_mov_b32_e32 v198, 1.0
	v_mfma_f32_32x32x16_bf16 v[16:31], v[76:79], v[222:225], v[16:31]
	v_cmp_ge_f32_e64 s[0:1], s56, v64
	s_cmp_eq_u64 s[0:1], exec
	s_cbranch_scc1 .Lc1_792
	s_branch .Lc1_801

.Lc1_792:
	v_exp_f32_e32 v197, v96
	v_exp_f32_e32 v208, v97
	v_exp_f32_e32 v209, v98
	v_exp_f32_e32 v210, v99
	v_exp_f32_e32 v211, v100
	v_exp_f32_e32 v220, v101
	v_exp_f32_e32 v221, v102
	v_exp_f32_e32 v222, v103
	v_exp_f32_e32 v223, v104
	v_exp_f32_e32 v224, v105
	v_exp_f32_e32 v225, v106
	v_exp_f32_e32 v226, v107
	v_exp_f32_e32 v227, v108
	v_exp_f32_e32 v228, v109
	v_exp_f32_e32 v229, v110
	v_exp_f32_e32 v230, v111
	s_waitcnt vmcnt(4) lgkmcnt(0)
	s_barrier
	ds_read_b128 v[64:67], v134 offset:33792
	ds_read_b128 v[68:71], v134 offset:41984
	ds_read_b128 v[200:203], v135 offset:33792
	ds_read_b128 v[204:207], v135 offset:41984
	v_exp_f32_e32 v231, v87
	s_waitcnt lgkmcnt(2)
	v_mfma_f32_32x32x16_bf16 v[96:111], v[64:67], v[122:125], 0
	v_exp_f32_e32 v232, v88
	v_exp_f32_e32 v233, v89
	v_exp_f32_e32 v234, v90
	v_exp_f32_e32 v235, v91
	v_exp_f32_e32 v236, v92
	v_exp_f32_e32 v237, v93
	v_exp_f32_e32 v238, v94
	v_mfma_f32_32x32x16_bf16 v[64:79], v[68:71], v[122:125], 0
	v_exp_f32_e32 v95, v95
	s_waitcnt lgkmcnt(0)
	v_mfma_f32_32x32x16_bf16 v[96:111], v[200:203], v[126:129], v[96:111]
	v_mfma_f32_32x32x16_bf16 v[64:79], v[204:207], v[126:129], v[64:79]
	ds_read_b128 v[200:203], v136 offset:33792
	ds_read_b128 v[204:207], v136 offset:41984
	s_waitcnt lgkmcnt(0)
	v_mfma_f32_32x32x16_bf16 v[96:111], v[200:203], v[118:121], v[96:111]
	v_mfma_f32_32x32x16_bf16 v[64:79], v[204:207], v[118:121], v[64:79]
	ds_read_b128 v[200:203], v137 offset:33792
	ds_read_b128 v[204:207], v137 offset:41984
	s_waitcnt lgkmcnt(0)
	v_mfma_f32_32x32x16_bf16 v[96:111], v[200:203], v[114:117], v[96:111]
	v_exp_f32_e32 v201, v80
	v_add_f32_e32 v80, v208, v197
	v_add_f32_e32 v199, v209, v210
	v_add_f32_e32 v80, v211, v80
	v_add_f32_e32 v199, v220, v199
	v_add_f32_e32 v80, v221, v80
	v_add_f32_e32 v199, v222, v199
	v_add_f32_e32 v80, v223, v80
	v_add_f32_e32 v199, v224, v199
	v_add_f32_e32 v80, v225, v80
	v_add_f32_e32 v199, v226, v199
	v_add_f32_e32 v80, v227, v80
	v_exp_f32_e32 v202, v81
	v_add_f32_e32 v199, v228, v199
	v_exp_f32_e32 v203, v82
	v_add_f32_e32 v80, v229, v80
	v_mfma_f32_32x32x16_bf16 v[64:79], v[204:207], v[114:117], v[64:79]
	v_exp_f32_e32 v204, v83
	v_add_f32_e32 v199, v230, v199
	v_exp_f32_e32 v205, v84
	v_add_f32_e32 v80, v201, v80
	v_exp_f32_e32 v206, v85
	v_add_f32_e32 v199, v202, v199
	v_exp_f32_e32 v207, v86
	v_add_f32_e32 v80, v203, v80
	v_add_f32_e32 v199, v204, v199
	v_add_f32_e32 v80, v205, v80
	v_add_f32_e32 v199, v206, v199
	v_add_f32_e32 v80, v207, v80
	v_add_f32_e32 v199, v231, v199
	v_add_f32_e32 v80, v232, v80
	v_add_f32_e32 v199, v233, v199
	v_add_f32_e32 v80, v234, v80
	v_add_f32_e32 v199, v235, v199
	v_add_f32_e32 v80, v236, v80
	v_add_f32_e32 v199, v237, v199
	v_add_f32_e32 v80, v238, v80
	v_add_f32_e32 v199, v95, v199
	v_add_f32_e32 v199, v199, v80
	v_cvt_pk_bf16_f32 v80, v197, v208
	v_cvt_pk_bf16_f32 v81, v209, v210
	v_cvt_pk_bf16_f32 v82, v211, v220
	v_cvt_pk_bf16_f32 v83, v221, v222
	v_cvt_pk_bf16_f32 v84, v223, v224
	v_cvt_pk_bf16_f32 v85, v225, v226
	v_cvt_pk_bf16_f32 v86, v227, v228
	v_cvt_pk_bf16_f32 v87, v229, v230
	v_cvt_pk_bf16_f32 v88, v201, v202
	v_cvt_pk_bf16_f32 v89, v203, v204
	v_cvt_pk_bf16_f32 v90, v205, v206
	v_cvt_pk_bf16_f32 v91, v207, v231
	v_cvt_pk_bf16_f32 v92, v232, v233
	v_cvt_pk_bf16_f32 v93, v234, v235
	v_cvt_pk_bf16_f32 v94, v236, v237
	v_cvt_pk_bf16_f32 v95, v238, v95
	s_add_i32 m0, s84, 0x8400
	s_add_u32 s66, s78, s65
	s_addc_u32 s67, s79, 0
	global_load_lds_dwordx4 v185, s[66:67]
	s_add_i32 m0, s84, 0xa400
	s_add_i32 s64, s65, 0x60000
	global_load_lds_dwordx4 v184, s[66:67]
	s_add_i32 m0, s84, 0xc400
	s_add_u32 s70, s80, s64
	s_addc_u32 s71, s81, 0
	global_load_lds_dwordx4 v183, s[70:71]
	s_add_i32 m0, s84, 0xe400
	s_mov_b32 s65, s64
	global_load_lds_dwordx4 v182, s[70:71]

.Lc1_799:
	v_exp_f32_e32 v159, v96
	v_exp_f32_e32 v161, v97
	v_exp_f32_e32 v157, v98
	v_exp_f32_e32 v160, v99
	v_exp_f32_e32 v155, v100
	v_exp_f32_e32 v158, v101
	v_exp_f32_e32 v154, v102
	v_exp_f32_e32 v156, v103
	v_exp_f32_e32 v151, v104
	v_exp_f32_e32 v153, v105
	v_exp_f32_e32 v149, v106
	v_exp_f32_e32 v152, v107
	v_exp_f32_e32 v147, v108
	v_exp_f32_e32 v150, v109
	v_exp_f32_e32 v146, v110
	v_exp_f32_e32 v148, v111
	v_fma_f32 v80, v193, v179, v195
	v_fma_f32 v179, v80, v198, v199
	v_mov_b32_e32 v193, v197
	s_cmp_gt_u32 s55, 30
	s_waitcnt vmcnt(4) lgkmcnt(0)
	s_barrier
	s_cbranch_scc1 .LBB0_803
	ds_read_b128 v[80:83], v134 offset:50176
	ds_read_b128 v[84:87], v134 offset:58368
	ds_read_b128 v[196:199], v135 offset:50176
	ds_read_b128 v[200:203], v135 offset:58368
	s_waitcnt lgkmcnt(2)
	v_mfma_f32_32x32x16_bf16 v[96:111], v[80:83], v[122:125], 0
	v_exp_f32_e32 v204, v72
	v_exp_f32_e32 v205, v73
	v_exp_f32_e32 v206, v74
	v_exp_f32_e32 v207, v75
	v_exp_f32_e32 v208, v76
	v_exp_f32_e32 v209, v77
	v_mfma_f32_32x32x16_bf16 v[80:95], v[84:87], v[122:125], 0
	v_exp_f32_e32 v210, v78
	v_exp_f32_e32 v79, v79
	s_waitcnt lgkmcnt(0)
	v_mfma_f32_32x32x16_bf16 v[96:111], v[196:199], v[126:129], v[96:111]
	v_mfma_f32_32x32x16_bf16 v[80:95], v[200:203], v[126:129], v[80:95]
	ds_read_b128 v[196:199], v136 offset:50176
	ds_read_b128 v[200:203], v136 offset:58368
	s_waitcnt lgkmcnt(0)
	v_mfma_f32_32x32x16_bf16 v[96:111], v[196:199], v[118:121], v[96:111]
	v_mfma_f32_32x32x16_bf16 v[80:95], v[200:203], v[118:121], v[80:95]
	ds_read_b128 v[196:199], v137 offset:50176
	ds_read_b128 v[200:203], v137 offset:58368
	v_exp_f32_e32 v180, v64
	v_add_f32_e32 v64, v161, v159
	v_add_f32_e32 v195, v157, v160
	v_add_f32_e32 v64, v155, v64
	v_add_f32_e32 v195, v158, v195
	v_add_f32_e32 v64, v154, v64
	v_add_f32_e32 v195, v156, v195
	v_add_f32_e32 v64, v151, v64
	v_add_f32_e32 v195, v153, v195
	v_add_f32_e32 v64, v149, v64
	v_add_f32_e32 v195, v152, v195
	v_add_f32_e32 v64, v147, v64
	s_waitcnt lgkmcnt(0)
	v_mfma_f32_32x32x16_bf16 v[96:111], v[196:199], v[114:117], v[96:111]
	v_exp_f32_e32 v197, v65
	v_add_f32_e32 v195, v150, v195
	v_exp_f32_e32 v198, v66
	v_add_f32_e32 v64, v146, v64
	v_exp_f32_e32 v199, v67
	v_add_f32_e32 v195, v148, v195
	v_add_f32_e32 v64, v180, v64
	v_mfma_f32_32x32x16_bf16 v[80:95], v[200:203], v[114:117], v[80:95]
	v_exp_f32_e32 v200, v68
	v_exp_f32_e32 v201, v69
	v_add_f32_e32 v195, v197, v195
	v_exp_f32_e32 v202, v70
	v_add_f32_e32 v64, v198, v64
	v_exp_f32_e32 v203, v71
	v_add_f32_e32 v195, v199, v195
	v_add_f32_e32 v64, v200, v64
	v_add_f32_e32 v195, v201, v195
	v_add_f32_e32 v64, v202, v64
	v_add_f32_e32 v195, v203, v195
	v_add_f32_e32 v64, v204, v64
	v_add_f32_e32 v195, v205, v195
	v_add_f32_e32 v64, v206, v64
	v_add_f32_e32 v195, v207, v195
	v_add_f32_e32 v64, v208, v64
	v_add_f32_e32 v195, v209, v195
	v_add_f32_e32 v64, v210, v64
	v_add_f32_e32 v195, v79, v195
	v_add_f32_e32 v195, v195, v64
	v_cvt_pk_bf16_f32 v64, v159, v161
	v_cvt_pk_bf16_f32 v65, v157, v160
	v_cvt_pk_bf16_f32 v66, v155, v158
	v_cvt_pk_bf16_f32 v67, v154, v156
	v_cvt_pk_bf16_f32 v68, v151, v153
	v_cvt_pk_bf16_f32 v69, v149, v152
	v_cvt_pk_bf16_f32 v70, v147, v150
	v_cvt_pk_bf16_f32 v71, v146, v148
	v_cvt_pk_bf16_f32 v72, v180, v197
	v_cvt_pk_bf16_f32 v73, v198, v199
	v_cvt_pk_bf16_f32 v74, v200, v201
	v_cvt_pk_bf16_f32 v75, v202, v203
	v_cvt_pk_bf16_f32 v76, v204, v205
	v_cvt_pk_bf16_f32 v77, v206, v207
	v_cvt_pk_bf16_f32 v78, v208, v209
	v_cvt_pk_bf16_f32 v79, v210, v79
	s_add_i32 m0, s84, 0x400
	s_add_u32 s66, s78, s65
	s_addc_u32 s67, s79, 0
	global_load_lds_dwordx4 v185, s[66:67]
	s_add_i32 m0, s84, 0x2400
	s_add_i32 s64, s65, 0x60000
	global_load_lds_dwordx4 v184, s[66:67]
	s_add_i32 m0, s84, 0x10400
	s_add_u32 s70, s80, s64
	s_addc_u32 s71, s81, 0
	global_load_lds_dwordx4 v183, s[70:71]
	s_add_i32 m0, s84, 0x12400
	s_mov_b32 s65, s64
	global_load_lds_dwordx4 v182, s[70:71]
	ds_read_b64_tr_b16 v[198:199], v192 offset:17408
	ds_read_b64_tr_b16 v[200:201], v192 offset:19456
	ds_read_b64_tr_b16 v[202:203], v192 offset:21504
	ds_read_b64_tr_b16 v[204:205], v192 offset:23552
	ds_read_b64_tr_b16 v[206:207], v192 offset:25600
	ds_read_b64_tr_b16 v[208:209], v192 offset:27648
	ds_read_b64_tr_b16 v[222:223], v192 offset:29696
	ds_read_b64_tr_b16 v[224:225], v192 offset:31744
	s_waitcnt lgkmcnt(0)
	v_mfma_f32_32x32x16_bf16 v[0:15], v[64:67], v[198:201], v[0:15]
	ds_read_b64_tr_b16 v[198:199], v192 offset:17920
	ds_read_b64_tr_b16 v[200:201], v192 offset:19968
	v_mfma_f32_32x32x16_bf16 v[0:15], v[68:71], v[202:205], v[0:15]
	ds_read_b64_tr_b16 v[202:203], v192 offset:22016
	ds_read_b64_tr_b16 v[204:205], v192 offset:24064
	v_mfma_f32_32x32x16_bf16 v[0:15], v[72:75], v[206:209], v[0:15]
	ds_read_b64_tr_b16 v[206:207], v192 offset:26112
	ds_read_b64_tr_b16 v[208:209], v192 offset:28160
	v_mfma_f32_32x32x16_bf16 v[0:15], v[76:79], v[222:225], v[0:15]
	ds_read_b64_tr_b16 v[222:223], v192 offset:30208
	ds_read_b64_tr_b16 v[224:225], v192 offset:32256
	s_waitcnt lgkmcnt(0)
	v_mfma_f32_32x32x16_bf16 v[48:63], v[64:67], v[198:201], v[48:63]
	ds_read_b64_tr_b16 v[198:199], v192 offset:18432
	ds_read_b64_tr_b16 v[200:201], v192 offset:20480
	v_mfma_f32_32x32x16_bf16 v[48:63], v[68:71], v[202:205], v[48:63]
	ds_read_b64_tr_b16 v[202:203], v192 offset:22528
	ds_read_b64_tr_b16 v[204:205], v192 offset:24576
	v_mfma_f32_32x32x16_bf16 v[48:63], v[72:75], v[206:209], v[48:63]
	ds_read_b64_tr_b16 v[206:207], v192 offset:26624
	ds_read_b64_tr_b16 v[208:209], v192 offset:28672
	v_mfma_f32_32x32x16_bf16 v[48:63], v[76:79], v[222:225], v[48:63]
	ds_read_b64_tr_b16 v[222:223], v192 offset:30720
	ds_read_b64_tr_b16 v[224:225], v192 offset:32768
	s_waitcnt lgkmcnt(0)
	v_mfma_f32_32x32x16_bf16 v[32:47], v[64:67], v[198:201], v[32:47]
	ds_read_b64_tr_b16 v[198:199], v192 offset:18944
	ds_read_b64_tr_b16 v[200:201], v192 offset:20992
	v_mfma_f32_32x32x16_bf16 v[32:47], v[68:71], v[202:205], v[32:47]
	ds_read_b64_tr_b16 v[202:203], v192 offset:23040
	ds_read_b64_tr_b16 v[204:205], v192 offset:25088
	v_mfma_f32_32x32x16_bf16 v[32:47], v[72:75], v[206:209], v[32:47]
	ds_read_b64_tr_b16 v[206:207], v192 offset:27136
	ds_read_b64_tr_b16 v[208:209], v192 offset:29184
	v_mfma_f32_32x32x16_bf16 v[32:47], v[76:79], v[222:225], v[32:47]
	ds_read_b64_tr_b16 v[222:223], v192 offset:31232
	ds_read_b64_tr_b16 v[224:225], v192 offset:33280
	s_waitcnt lgkmcnt(0)
	v_mfma_f32_32x32x16_bf16 v[16:31], v[64:67], v[198:201], v[16:31]
	v_max_f32_e32 v64, v96, v97
	v_max3_f32 v65, v80, v81, v82
	v_max3_f32 v64, v64, v98, v99
	v_max3_f32 v65, v65, v83, v84
	v_max3_f32 v64, v64, v100, v101
	v_mfma_f32_32x32x16_bf16 v[16:31], v[68:71], v[202:205], v[16:31]
	v_max3_f32 v65, v65, v85, v86
	v_max3_f32 v64, v64, v102, v103
	v_max3_f32 v65, v65, v87, v88
	v_max3_f32 v64, v64, v104, v105
	v_max3_f32 v65, v65, v89, v90
	v_max3_f32 v64, v64, v106, v107
	v_max3_f32 v65, v65, v91, v92
	v_mfma_f32_32x32x16_bf16 v[16:31], v[72:75], v[206:209], v[16:31]
	v_max3_f32 v64, v64, v108, v109
	v_max3_f32 v65, v65, v93, v94
	v_max3_f32 v64, v64, v110, v111
	v_max3_f32 v64, v64, v65, v95
	v_mov_b32_e32 v198, 1.0
	v_mfma_f32_32x32x16_bf16 v[16:31], v[76:79], v[222:225], v[16:31]
	v_cmp_ge_f32_e64 s[0:1], s56, v64
	s_cmp_eq_u64 s[0:1], exec
	s_cbranch_scc1 .Lc2_792
	s_branch .Lc2_801

.Lc2_792:
	v_exp_f32_e32 v197, v96
	v_exp_f32_e32 v208, v97
	v_exp_f32_e32 v209, v98
	v_exp_f32_e32 v210, v99
	v_exp_f32_e32 v211, v100
	v_exp_f32_e32 v220, v101
	v_exp_f32_e32 v221, v102
	v_exp_f32_e32 v222, v103
	v_exp_f32_e32 v223, v104
	v_exp_f32_e32 v224, v105
	v_exp_f32_e32 v225, v106
	v_exp_f32_e32 v226, v107
	v_exp_f32_e32 v227, v108
	v_exp_f32_e32 v228, v109
	v_exp_f32_e32 v229, v110
	v_exp_f32_e32 v230, v111
	s_waitcnt vmcnt(4) lgkmcnt(0)
	s_barrier
	ds_read_b128 v[64:67], v130 offset:50176
	ds_read_b128 v[68:71], v130 offset:58368
	ds_read_b128 v[200:203], v131 offset:50176
	ds_read_b128 v[204:207], v131 offset:58368
	v_exp_f32_e32 v231, v87
	s_waitcnt lgkmcnt(2)
	v_mfma_f32_32x32x16_bf16 v[96:111], v[64:67], v[122:125], 0
	v_exp_f32_e32 v232, v88
	v_exp_f32_e32 v233, v89
	v_exp_f32_e32 v234, v90
	v_exp_f32_e32 v235, v91
	v_exp_f32_e32 v236, v92
	v_exp_f32_e32 v237, v93
	v_exp_f32_e32 v238, v94
	v_mfma_f32_32x32x16_bf16 v[64:79], v[68:71], v[122:125], 0
	v_exp_f32_e32 v95, v95
	s_waitcnt lgkmcnt(0)
	v_mfma_f32_32x32x16_bf16 v[96:111], v[200:203], v[126:129], v[96:111]
	v_mfma_f32_32x32x16_bf16 v[64:79], v[204:207], v[126:129], v[64:79]
	ds_read_b128 v[200:203], v132 offset:50176
	ds_read_b128 v[204:207], v132 offset:58368
	s_waitcnt lgkmcnt(0)
	v_mfma_f32_32x32x16_bf16 v[96:111], v[200:203], v[118:121], v[96:111]
	v_mfma_f32_32x32x16_bf16 v[64:79], v[204:207], v[118:121], v[64:79]
	ds_read_b128 v[200:203], v133 offset:50176
	ds_read_b128 v[204:207], v133 offset:58368
	s_waitcnt lgkmcnt(0)
	v_mfma_f32_32x32x16_bf16 v[96:111], v[200:203], v[114:117], v[96:111]
	v_exp_f32_e32 v201, v80
	v_add_f32_e32 v80, v208, v197
	v_add_f32_e32 v199, v209, v210
	v_add_f32_e32 v80, v211, v80
	v_add_f32_e32 v199, v220, v199
	v_add_f32_e32 v80, v221, v80
	v_add_f32_e32 v199, v222, v199
	v_add_f32_e32 v80, v223, v80
	v_add_f32_e32 v199, v224, v199
	v_add_f32_e32 v80, v225, v80
	v_add_f32_e32 v199, v226, v199
	v_add_f32_e32 v80, v227, v80
	v_exp_f32_e32 v202, v81
	v_add_f32_e32 v199, v228, v199
	v_exp_f32_e32 v203, v82
	v_add_f32_e32 v80, v229, v80
	v_mfma_f32_32x32x16_bf16 v[64:79], v[204:207], v[114:117], v[64:79]
	v_exp_f32_e32 v204, v83
	v_add_f32_e32 v199, v230, v199
	v_exp_f32_e32 v205, v84
	v_add_f32_e32 v80, v201, v80
	v_exp_f32_e32 v206, v85
	v_add_f32_e32 v199, v202, v199
	v_exp_f32_e32 v207, v86
	v_add_f32_e32 v80, v203, v80
	v_add_f32_e32 v199, v204, v199
	v_add_f32_e32 v80, v205, v80
	v_add_f32_e32 v199, v206, v199
	v_add_f32_e32 v80, v207, v80
	v_add_f32_e32 v199, v231, v199
	v_add_f32_e32 v80, v232, v80
	v_add_f32_e32 v199, v233, v199
	v_add_f32_e32 v80, v234, v80
	v_add_f32_e32 v199, v235, v199
	v_add_f32_e32 v80, v236, v80
	v_add_f32_e32 v199, v237, v199
	v_add_f32_e32 v80, v238, v80
	v_add_f32_e32 v199, v95, v199
	v_add_f32_e32 v199, v199, v80
	v_cvt_pk_bf16_f32 v80, v197, v208
	v_cvt_pk_bf16_f32 v81, v209, v210
	v_cvt_pk_bf16_f32 v82, v211, v220
	v_cvt_pk_bf16_f32 v83, v221, v222
	v_cvt_pk_bf16_f32 v84, v223, v224
	v_cvt_pk_bf16_f32 v85, v225, v226
	v_cvt_pk_bf16_f32 v86, v227, v228
	v_cvt_pk_bf16_f32 v87, v229, v230
	v_cvt_pk_bf16_f32 v88, v201, v202
	v_cvt_pk_bf16_f32 v89, v203, v204
	v_cvt_pk_bf16_f32 v90, v205, v206
	v_cvt_pk_bf16_f32 v91, v207, v231
	v_cvt_pk_bf16_f32 v92, v232, v233
	v_cvt_pk_bf16_f32 v93, v234, v235
	v_cvt_pk_bf16_f32 v94, v236, v237
	v_cvt_pk_bf16_f32 v95, v238, v95
	s_add_i32 m0, s84, 0x4400
	s_add_u32 s66, s78, s65
	s_addc_u32 s67, s79, 0
	global_load_lds_dwordx4 v185, s[66:67]
	s_add_i32 m0, s84, 0x6400
	s_add_i32 s64, s65, 0x60000
	global_load_lds_dwordx4 v184, s[66:67]
	s_cmp_eq_u32 s55, 25
	s_cselect_b32 s64, s89, s64
	s_add_i32 m0, s84, 0x14400
	s_add_u32 s70, s80, s64
	s_addc_u32 s71, s81, 0
	global_load_lds_dwordx4 v183, s[70:71]
	s_add_i32 m0, s84, 0x16400
	s_mov_b32 s65, s64
	global_load_lds_dwordx4 v182, s[70:71]

.Lc2_799:
	v_exp_f32_e32 v159, v96
	v_exp_f32_e32 v161, v97
	v_exp_f32_e32 v157, v98
	v_exp_f32_e32 v160, v99
	v_exp_f32_e32 v155, v100
	v_exp_f32_e32 v158, v101
	v_exp_f32_e32 v154, v102
	v_exp_f32_e32 v156, v103
	v_exp_f32_e32 v151, v104
	v_exp_f32_e32 v153, v105
	v_exp_f32_e32 v149, v106
	v_exp_f32_e32 v152, v107
	v_exp_f32_e32 v147, v108
	v_exp_f32_e32 v150, v109
	v_exp_f32_e32 v146, v110
	v_exp_f32_e32 v148, v111
	v_fma_f32 v80, v193, v179, v195
	v_fma_f32 v179, v80, v198, v199
	v_mov_b32_e32 v193, v197
	s_add_i32 s55, s55, 6
	s_waitcnt vmcnt(4) lgkmcnt(0)
	s_barrier
	s_branch .LBB0_787
